# v59: v58 + m0 save/restore removed around the in-loop attention LDS-DMA issues (12 SALU per tile-step)
# speedup vs baseline: 1.0033x; 1.0033x over previous
.LBB0_1049:
	s_add_i32 s14, s86, 3
	s_min_i32 s4, s14, s78
	s_ashr_i32 s5, s4, 31
	s_lshl_b64 s[12:13], s[4:5], 16
	s_and_b32 s5, s14, 3
	s_mulk_i32 s5, 0x3000
	v_lshl_add_u64 v[196:197], v[110:111], 0, s[12:13]
	s_add_i32 s12, s5, s85
	s_mov_b32 m0, s12
	s_nop 0
	global_load_lds_dwordx4 v[196:197], off
	s_and_b64 vcc, exec, s[8:9]
	s_cbranch_vccnz .Lmla_dma_v3
	v_mad_i64_i32 v[196:197], s[12:13], s4, v235, v[112:113]
	v_readlane_b32 s4, v254, 28
	s_add_i32 s4, s5, s4
	s_mov_b32 m0, s4
	s_nop 0
	global_load_lds_dwordx4 v[196:197], off
.Lmla_dma_v3:
	s_add_i32 s12, s86, 2
	s_min_i32 s12, s12, s78
	s_ashr_i32 s13, s12, 31
	s_add_i32 s15, s80, 0x6000
	s_lshl_b64 s[12:13], s[12:13], 16
	s_and_b32 s15, s15, 0x6000
	v_readlane_b32 s16, v254, 34
	s_add_i32 s15, s15, s16
	v_lshl_add_u64 v[196:197], v[114:115], 0, s[12:13]
	s_mov_b32 m0, s15
	s_nop 0
	global_load_lds_dwordx4 v[196:197], off
	s_add_i32 s4, s81, s83
	s_addk_i32 s80, 0x2000
	s_add_i32 s82, s82, 64
	v_subrev_u32_e32 v122, 64, v122
	s_and_b64 vcc, exec, s[6:7]
	s_cbranch_vccz .LBB0_1056

.LBB0_1100:
	global_load_dword v175, v1, s[94:95] offset:4
	s_add_i32 s5, s78, 3
	s_min_i32 s5, s5, s81
	v_mad_i64_i32 v[200:201], s[12:13], s5, v235, v[182:183]
	s_add_i32 s5, s89, 0x2000
	s_and_b32 s5, s5, 0x6000
	s_add_i32 s5, s5, s85
	s_mov_b32 m0, s5
	s_nop 0
	global_load_lds_dwordx4 v[200:201], off
	s_add_i32 s5, s78, 2
	s_min_i32 s5, s5, s81
	s_add_i32 s12, s88, 0xc000
	s_and_b32 s15, s12, 0xc000
	v_mad_i64_i32 v[200:201], s[12:13], s5, v235, v[150:151]
	s_add_i32 s12, s15, s75
	s_mov_b32 m0, s12
	s_nop 0
	global_load_lds_dwordx4 v[200:201], off
	v_mad_i64_i32 v[200:201], s[12:13], s5, v235, v[152:153]
	s_add_i32 s5, s15, s74
	s_mov_b32 m0, s5
	s_nop 0
	global_load_lds_dwordx4 v[200:201], off
	s_add_u32 s94, s94, 4
	s_addc_u32 s95, s95, 0
	s_addk_i32 s89, 0x2000
	s_add_i32 s5, s1, s4
	s_addk_i32 s88, 0x4000
	s_add_i32 s93, s93, 64
	v_subrev_u32_e32 v169, 64, v169
	v_add_u32_e32 v167, 0x100, v167
	s_and_b64 vcc, exec, s[6:7]
	s_cbranch_vccz .LBB0_1107
